# v74 + attention queue order: lightest differential items (query blocks 3..0) served last so the phase tail consists of short items
# baseline (speedup 1.0000x reference)
.LBB0_3607:
	s_or_b64 exec, exec, s[4:5]
	v_mov_b32_e32 v0, s59
	s_waitcnt lgkmcnt(0)
	s_barrier
	ds_read_b32 v0, v0
	v_readlane_b32 s2, v254, 55
	v_readlane_b32 s3, v254, 56
	s_xor_b64 s[40:41], s[2:3], -1
	s_waitcnt lgkmcnt(0)
	v_readfirstlane_b32 s69, v0
	s_cmpk_lt_i32 s69, 0x200
	s_cbranch_scc1 .Lqo_done
	s_cmpk_gt_i32 s69, 0x67f
	s_cbranch_scc1 .Lqo_done
	s_cmpk_lt_i32 s69, 0x600
	s_cbranch_scc1 .Lqo_mid
	s_addk_i32 s69, 0xfc00
	s_branch .Lqo_done
.Lqo_mid:
	s_addk_i32 s69, 0x80
.Lqo_done:
	s_cmpk_gt_i32 s69, 0x67f
	s_cselect_b64 s[86:87], -1, 0
	s_and_b64 vcc, exec, s[86:87]
	s_barrier
	s_cbranch_vccnz .LBB0_3602
	v_mov_b32_e32 v154, v147
	s_mov_b64 s[6:7], -1
	v_readfirstlane_b32 s33, v154
	s_ashr_i32 s79, s33, 6
	v_and_b32_e32 v153, 63, v154
	s_cmpk_gt_i32 s69, 0x7f
	s_cbranch_scc0 .LBB0_3774
	s_add_i32 s48, s69, 0xfffffd80
	s_cmpk_gt_u32 s48, 0x1ff
	s_mov_b64 s[4:5], -1
	s_cbranch_scc0 .LBB0_3657
	s_cmpk_gt_u32 s69, 0x27f
	s_cbranch_scc0 .LBB0_3635
	s_cmpk_lt_u32 s69, 0x480
	s_cbranch_scc1 .LBB0_3634
	v_readlane_b32 s2, v254, 58
	v_readlane_b32 s3, v254, 59
	s_load_dwordx2 s[4:5], s[2:3], 0x28
	s_add_i32 s0, s69, 0xfffffb80
	s_lshr_b32 s6, s0, 4
	s_sub_i32 s2, 31, s6
	v_readlane_b32 s8, v255, 34
	v_readlane_b32 s9, v255, 35
	s_waitcnt lgkmcnt(0)
	s_add_u32 s7, s4, s8
	s_addc_u32 s8, s5, s9
	s_and_b32 s0, s69, 1
	s_lshl_b32 s4, s0, 2
	s_ashr_i32 s5, s33, 7
	s_lshl_b32 s9, s79, 5
	s_add_i32 s4, s5, s4
	s_lshl_b32 s5, s2, 6
	s_and_b32 s9, s9, 32
	s_or_b32 s5, s9, s5
	s_bfe_u32 s3, s69, 0x30001
	v_and_or_b32 v119, v154, 31, s5
	v_lshl_or_b32 v118, s3, 11, v119
	v_readlane_b32 s10, v254, 60
	v_lshlrev_b32_e32 v0, 10, v118
	v_readlane_b32 s11, v254, 61
	s_lshl_b32 s42, s4, 6
	v_lshrrev_b32_e32 v2, 5, v153
	v_lshl_add_u64 v[4:5], s[10:11], 0, v[0:1]
	s_ashr_i32 s43, s42, 31
	v_lshl_add_u64 v[4:5], s[42:43], 1, v[4:5]
	v_lshlrev_b32_e32 v0, 4, v2
	s_ashr_i32 s5, s4, 31
	v_lshl_add_u64 v[4:5], v[4:5], 0, v[0:1]
	s_lshl_b64 s[4:5], s[4:5], 2
	global_load_dwordx4 v[66:69], v[4:5], off
	global_load_dwordx4 v[70:73], v[4:5], off offset:32
	global_load_dwordx4 v[74:77], v[4:5], off offset:64
	global_load_dwordx4 v[78:81], v[4:5], off offset:96
	s_add_u32 s4, s7, s4
	s_addc_u32 s5, s8, s5
	global_load_dword v0, v1, s[4:5]
	v_sub_u32_e64 v3, 29, s6 clamp
	s_min_u32 s4, s6, 29
	v_readfirstlane_b32 s5, v3
	s_max_u32 s5, s2, s5
	s_add_i32 s4, s4, s5
	s_sub_i32 s10, s4, 28
	s_cmp_lt_u32 s10, 2
	v_readfirstlane_b32 s4, v3
	s_cbranch_scc1 .LBB0_3616
	s_and_b32 s11, s10, -2
	s_add_i32 s5, s4, 1
	s_mov_b32 s6, 0
	s_mov_b32 s12, s11
	s_mov_b64 s[8:9], s[4:5]
	s_mov_b32 s7, s6
